# speedup vs baseline: 1.0212x; 1.0212x over previous
_Z16sum_layer_kernelPKfS0_Pf:
	s_load_dwordx4 s[4:7], s[0:1], 0x0
	s_load_dwordx2 s[8:9], s[0:1], 0x10
	v_lshrrev_b32_e32 v42, 6, v0
	v_bfe_u32 v41, v0, 5, 1
	v_and_b32_e32 v40, 31, v0
	v_readfirstlane_b32 s23, v42
	v_and_b32_e32 v43, 7, v0
	v_bfe_u32 v44, v0, 3, 3
	s_lshl_b32 s3, s2, 12
	s_lshl_b32 s19, s2, 7
	s_lshl_b32 s23, s23, 12
	v_lshlrev_b32_e32 v1, 11, v41
	v_lshl_or_b32 v1, v40, 2, v1
	s_mov_b32 m0, s23
	v_lshrrev_b32_e32 v46, 1, v44
	v_xor_b32_e32 v46, v43, v46
	v_lshlrev_b32_e32 v46, 4, v46
	v_lshl_add_u32 v35, v44, 16, v46
	v_lshl_add_u32 v35, v42, 21, v35
	v_add_u32_e32 v35, s19, v35
	v_xor_b32_e32 v86, 64, v35
	s_mov_b32 s20, 0x7fc00
	s_mov_b32 s21, 0xff800
	s_mov_b32 s22, 0x17f400
	s_mov_b32 s14, 0x200000
	s_mov_b32 s15, 0x20000
	v_and_b32_e32 v45, 63, v0
	v_lshlrev_b32_e32 v37, 4, v45
	s_add_u32 s54, s23, 0x4000
	s_waitcnt lgkmcnt(0)
	s_mov_b32 s12, s6
	s_and_b32 s13, s7, 0xffff
	s_and_b32 s5, s5, 0xffff
	s_mov_b32 s6, 0x800000
	s_mov_b32 s7, s15
	s_mov_b32 m0, s54
	s_nop 0
	buffer_load_dwordx4 v37, s[12:15], s3 offen lds
	buffer_load_dwordx4 v37, s[12:15], s3 offen offset:1024 lds
	buffer_load_dwordx4 v37, s[12:15], s3 offen offset:2048 lds
	buffer_load_dwordx4 v37, s[12:15], s3 offen offset:3072 lds
	s_mov_b32 m0, s23
	s_nop 0
	buffer_load_dwordx4 v35, s[4:7], 0 offen nt lds
	buffer_load_dwordx4 v86, s[4:7], s20 offen offset:1024 nt lds
	buffer_load_dwordx4 v35, s[4:7], s21 offen offset:2048 nt lds
	buffer_load_dwordx4 v86, s[4:7], s22 offen offset:3072 nt lds
	v_and_b32_e32 v45, 63, v0
	v_lshlrev_b32_e32 v36, 2, v40
	v_lshl_add_u32 v36, v41, 18, v36
	v_lshl_add_u32 v36, v42, 21, v36
	v_add_u32_e32 v36, s19, v36
	v_bfe_u32 v47, v40, 1, 3
	v_lshlrev_b32_e32 v39, 2, v41
	v_xor_b32_e32 v39, v39, v47
	v_lshlrev_b32_e32 v39, 4, v39
	v_lshl_add_u32 v39, v40, 7, v39
	v_lshl_add_u32 v39, v42, 12, v39
	v_xor_b32_e32 v81, 16, v39
	v_xor_b32_e32 v82, 32, v39
	v_xor_b32_e32 v83, 48, v39
	v_cmp_gt_u32_e32 vcc, 32, v45
	v_mov_b32_e32 v34, 0xc1600000
	v_mov_b32_e32 v84, 0x3fb8aa3b
	v_mov_b32_e32 v85, 0x3f317218
	s_lshl_b32 s24, 1, 16
	s_lshl_b32 s25, 2, 16
	s_lshl_b32 s26, 3, 16
	s_lshl_b32 s27, 8, 16
	s_lshl_b32 s28, 9, 16
	s_lshl_b32 s29, 10, 16
	s_lshl_b32 s30, 11, 16
	s_lshl_b32 s31, 16, 16
	s_lshl_b32 s32, 17, 16
	s_lshl_b32 s33, 18, 16
	s_lshl_b32 s34, 19, 16
	s_lshl_b32 s35, 24, 16
	s_lshl_b32 s36, 25, 16
	s_lshl_b32 s37, 26, 16
	s_lshl_b32 s38, 27, 16
	s_and_b32 s9, s9, 0xffff
	s_mov_b32 s10, s6
	s_mov_b32 s11, s15
	v_lshl_add_u32 v38, v42, 12, v1
	v_add_u32_e32 v38, 0x4000, v38
	v_add_u32_e32 v87, 0x400, v38
	s_waitcnt vmcnt(4)
	ds_read2_b32 v[18:19], v38 offset0:0 offset1:32
	ds_read2_b32 v[20:21], v38 offset0:64 offset1:96
	ds_read2_b32 v[22:23], v38 offset0:128 offset1:160
	ds_read2_b32 v[24:25], v38 offset0:192 offset1:224
	ds_read2_b32 v[26:27], v87 offset0:0 offset1:32
	ds_read2_b32 v[28:29], v87 offset0:64 offset1:96
	ds_read2_b32 v[30:31], v87 offset0:128 offset1:160
	ds_read2_b32 v[32:33], v87 offset0:192 offset1:224
	s_waitcnt lgkmcnt(0)
	v_max3_f32 v48, v18, v19, v20
	v_max3_f32 v50, v21, v22, v23
	v_max3_f32 v48, v48, v24, v25
	v_max3_f32 v50, v50, v26, v27
	v_max3_f32 v48, v48, v28, v29
	v_max3_f32 v50, v50, v30, v31
	v_max3_f32 v48, v48, v32, v33
	v_max_f32_e32 v48, v48, v50
	v_mov_b32_e32 v50, v48
	s_nop 1
	v_permlane32_swap_b32_e32 v48, v50
	v_max_f32_e32 v48, v48, v50
	v_fmamk_f32 v48, v48, 0x3fb8aa3b, v34
	v_pk_fma_f32 v[18:19], v[18:19], v[84:85], v[48:49] op_sel_hi:[1,0,0] neg_lo:[0,0,1] neg_hi:[0,0,1]
	v_exp_f32_e32 v18, v18
	v_exp_f32_e32 v19, v19
	v_pk_fma_f32 v[20:21], v[20:21], v[84:85], v[48:49] op_sel_hi:[1,0,0] neg_lo:[0,0,1] neg_hi:[0,0,1]
	v_exp_f32_e32 v20, v20
	v_exp_f32_e32 v21, v21
	v_pk_fma_f32 v[22:23], v[22:23], v[84:85], v[48:49] op_sel_hi:[1,0,0] neg_lo:[0,0,1] neg_hi:[0,0,1]
	v_exp_f32_e32 v22, v22
	v_exp_f32_e32 v23, v23
	v_pk_fma_f32 v[24:25], v[24:25], v[84:85], v[48:49] op_sel_hi:[1,0,0] neg_lo:[0,0,1] neg_hi:[0,0,1]
	v_exp_f32_e32 v24, v24
	v_exp_f32_e32 v25, v25
	v_pk_fma_f32 v[26:27], v[26:27], v[84:85], v[48:49] op_sel_hi:[1,0,0] neg_lo:[0,0,1] neg_hi:[0,0,1]
	v_exp_f32_e32 v26, v26
	v_exp_f32_e32 v27, v27
	v_pk_fma_f32 v[28:29], v[28:29], v[84:85], v[48:49] op_sel_hi:[1,0,0] neg_lo:[0,0,1] neg_hi:[0,0,1]
	v_exp_f32_e32 v28, v28
	v_exp_f32_e32 v29, v29
	v_pk_fma_f32 v[30:31], v[30:31], v[84:85], v[48:49] op_sel_hi:[1,0,0] neg_lo:[0,0,1] neg_hi:[0,0,1]
	v_exp_f32_e32 v30, v30
	v_exp_f32_e32 v31, v31
	v_pk_fma_f32 v[32:33], v[32:33], v[84:85], v[48:49] op_sel_hi:[1,0,0] neg_lo:[0,0,1] neg_hi:[0,0,1]
	v_exp_f32_e32 v32, v32
	v_exp_f32_e32 v33, v33
	v_pk_add_f32 v[56:57], v[18:19], v[20:21]
	v_pk_add_f32 v[58:59], v[22:23], v[24:25]
	v_pk_add_f32 v[60:61], v[26:27], v[28:29]
	v_pk_add_f32 v[62:63], v[30:31], v[32:33]
	v_pk_add_f32 v[56:57], v[56:57], v[58:59]
	v_pk_add_f32 v[60:61], v[60:61], v[62:63]
	v_pk_add_f32 v[56:57], v[56:57], v[60:61]
	v_add_f32_e32 v50, v56, v57
	v_mov_b32_e32 v51, v50
	s_nop 1
	v_permlane32_swap_b32_e32 v50, v51
	v_add_f32_e32 v50, v50, v51
	v_log_f32_e32 v50, v50
	v_cvt_pk_f16_f32 v40, v18, v19
	v_cvt_pk_f16_f32 v41, v20, v21
	v_cvt_pk_f16_f32 v42, v22, v23
	v_cvt_pk_f16_f32 v43, v24, v25
	v_cvt_pk_f16_f32 v44, v26, v27
	v_cvt_pk_f16_f32 v45, v28, v29
	v_cvt_pk_f16_f32 v46, v30, v31
	v_cvt_pk_f16_f32 v47, v32, v33
	v_add_f32_e32 v50, 0x41600000, v50
	v_mul_f32_e32 v50, 0xbf317218, v50
	v_cndmask_b32_e64 v51, v50, 1.0, vcc
	s_waitcnt vmcnt(0)
	ds_read_b128 v[2:5], v39
	ds_read_b128 v[6:9], v81
	ds_read_b128 v[10:13], v82
	ds_read_b128 v[14:17], v83
	s_waitcnt lgkmcnt(2)
	v_max3_f32 v52, v2, v3, v4
	v_max3_f32 v53, v5, v6, v7
	v_max_f32_e32 v52, v52, v8
	v_max_f32_e32 v53, v53, v9
	s_waitcnt lgkmcnt(0)
	v_max3_f32 v52, v52, v10, v11
	v_max3_f32 v53, v53, v12, v13
	v_max3_f32 v52, v52, v14, v15
	v_max3_f32 v53, v53, v16, v17
	v_max_f32_e32 v52, v52, v53
	v_mov_b32_e32 v53, v52
	s_nop 1
	v_permlane32_swap_b32_e32 v52, v53
	v_max_f32_e32 v52, v52, v53
	v_cndmask_b32_e32 v54, 1.0, v52, vcc
	v_fmamk_f32 v48, v52, 0x3fb8aa3b, v34
	v_pk_fma_f32 v[2:3], v[2:3], v[84:85], v[48:49] op_sel_hi:[1,0,0] neg_lo:[0,0,1] neg_hi:[0,0,1]
	v_mfma_f32_32x32x2_f32 v[64:79], v54, v51, 0
	v_exp_f32_e32 v2, v2
	v_exp_f32_e32 v3, v3
	v_pk_fma_f32 v[4:5], v[4:5], v[84:85], v[48:49] op_sel_hi:[1,0,0] neg_lo:[0,0,1] neg_hi:[0,0,1]
	v_exp_f32_e32 v4, v4
	v_exp_f32_e32 v5, v5
	v_pk_fma_f32 v[6:7], v[6:7], v[84:85], v[48:49] op_sel_hi:[1,0,0] neg_lo:[0,0,1] neg_hi:[0,0,1]
	v_exp_f32_e32 v6, v6
	v_exp_f32_e32 v7, v7
	v_pk_fma_f32 v[8:9], v[8:9], v[84:85], v[48:49] op_sel_hi:[1,0,0] neg_lo:[0,0,1] neg_hi:[0,0,1]
	v_exp_f32_e32 v8, v8
	v_exp_f32_e32 v9, v9
	v_pk_fma_f32 v[10:11], v[10:11], v[84:85], v[48:49] op_sel_hi:[1,0,0] neg_lo:[0,0,1] neg_hi:[0,0,1]
	v_exp_f32_e32 v10, v10
	v_cvt_pk_f16_f32 v56, v2, v3
	v_cvt_pk_f16_f32 v57, v4, v5
	v_cvt_pk_f16_f32 v58, v6, v7
	v_cvt_pk_f16_f32 v59, v8, v9
	v_exp_f32_e32 v11, v11
	v_pk_fma_f32 v[12:13], v[12:13], v[84:85], v[48:49] op_sel_hi:[1,0,0] neg_lo:[0,0,1] neg_hi:[0,0,1]
	v_exp_f32_e32 v12, v12
	v_mfma_f32_32x32x16_f16 v[18:33], v[56:59], v[40:43], 0
	v_exp_f32_e32 v13, v13
	v_pk_fma_f32 v[14:15], v[14:15], v[84:85], v[48:49] op_sel_hi:[1,0,0] neg_lo:[0,0,1] neg_hi:[0,0,1]
	v_exp_f32_e32 v14, v14
	v_exp_f32_e32 v15, v15
	v_pk_fma_f32 v[16:17], v[16:17], v[84:85], v[48:49] op_sel_hi:[1,0,0] neg_lo:[0,0,1] neg_hi:[0,0,1]
	v_exp_f32_e32 v16, v16
	v_exp_f32_e32 v17, v17
	v_cvt_pk_f16_f32 v60, v10, v11
	v_cvt_pk_f16_f32 v61, v12, v13
	v_cvt_pk_f16_f32 v62, v14, v15
	v_cvt_pk_f16_f32 v63, v16, v17
	s_nop 1
	v_mfma_f32_32x32x16_f16 v[18:33], v[60:63], v[44:47], v[18:33]
	s_nop 11
	v_log_f32_e32 v18, v18
	v_log_f32_e32 v19, v19
	v_log_f32_e32 v20, v20
	v_log_f32_e32 v21, v21
	v_log_f32_e32 v22, v22
	v_log_f32_e32 v23, v23
	v_pk_fma_f32 v[64:65], v[18:19], v[84:85], v[64:65] op_sel:[0,1,0] op_sel_hi:[1,1,1]
	buffer_store_dword v64, v36, s[8:11], 0 offen
	buffer_store_dword v65, v36, s[8:11], s24 offen
	v_log_f32_e32 v24, v24
	v_log_f32_e32 v25, v25
	v_pk_fma_f32 v[66:67], v[20:21], v[84:85], v[66:67] op_sel:[0,1,0] op_sel_hi:[1,1,1]
	buffer_store_dword v66, v36, s[8:11], s25 offen
	buffer_store_dword v67, v36, s[8:11], s26 offen
	v_log_f32_e32 v26, v26
	v_log_f32_e32 v27, v27
	v_pk_fma_f32 v[68:69], v[22:23], v[84:85], v[68:69] op_sel:[0,1,0] op_sel_hi:[1,1,1]
	buffer_store_dword v68, v36, s[8:11], s27 offen
	buffer_store_dword v69, v36, s[8:11], s28 offen
	v_log_f32_e32 v28, v28
	v_log_f32_e32 v29, v29
	v_pk_fma_f32 v[70:71], v[24:25], v[84:85], v[70:71] op_sel:[0,1,0] op_sel_hi:[1,1,1]
	buffer_store_dword v70, v36, s[8:11], s29 offen
	buffer_store_dword v71, v36, s[8:11], s30 offen
	v_log_f32_e32 v30, v30
	v_log_f32_e32 v31, v31
	v_pk_fma_f32 v[72:73], v[26:27], v[84:85], v[72:73] op_sel:[0,1,0] op_sel_hi:[1,1,1]
	buffer_store_dword v72, v36, s[8:11], s31 offen
	buffer_store_dword v73, v36, s[8:11], s32 offen
	v_log_f32_e32 v32, v32
	v_log_f32_e32 v33, v33
	v_pk_fma_f32 v[74:75], v[28:29], v[84:85], v[74:75] op_sel:[0,1,0] op_sel_hi:[1,1,1]
	buffer_store_dword v74, v36, s[8:11], s33 offen
	buffer_store_dword v75, v36, s[8:11], s34 offen
	v_pk_fma_f32 v[76:77], v[30:31], v[84:85], v[76:77] op_sel:[0,1,0] op_sel_hi:[1,1,1]
	buffer_store_dword v76, v36, s[8:11], s35 offen
	buffer_store_dword v77, v36, s[8:11], s36 offen
	v_pk_fma_f32 v[78:79], v[32:33], v[84:85], v[78:79] op_sel:[0,1,0] op_sel_hi:[1,1,1]
	buffer_store_dword v78, v36, s[8:11], s37 offen
	buffer_store_dword v79, v36, s[8:11], s38 offen
	s_endpgm
